# second conformer conv variant (4 outputs per lane): its 26 serialised LDS tap reads also kept 8 deep with counted waits
# baseline (speedup 1.0000x reference)
.LBB0_2186:
	s_or_b64 exec, exec, s[10:11]
	s_waitcnt vmcnt(32)
	v_lshlrev_b32_e32 v18, 2, v29
	v_lshl_add_u32 v29, v22, 1, 0
	global_load_dwordx4 v[2:5], v18, s[18:19] offset:16
	global_load_dwordx4 v[10:13], v18, s[18:19]
	global_load_dwordx4 v[6:9], v18, s[16:17] offset:16
	global_load_dwordx4 v[14:17], v18, s[16:17]
	s_waitcnt lgkmcnt(0)
	s_barrier
	ds_read_u16 v21, v29
	ds_read_u16 v24, v29 offset:1024
	ds_read_u16 v25, v29 offset:2048
	ds_read_u16 v27, v29 offset:3072
	ds_read_u16 v30, v29 offset:4096
	s_waitcnt lgkmcnt(4)
	v_lshlrev_b32_e32 v21, 16, v21
	s_waitcnt vmcnt(4)
	v_fma_f32 v21, v50, v21, v23
	s_waitcnt lgkmcnt(3)
	v_lshlrev_b32_e32 v24, 16, v24
	v_fmac_f32_e32 v21, v41, v24
	v_fma_f32 v24, v50, v24, v23
	s_waitcnt lgkmcnt(2)
	v_lshlrev_b32_e32 v25, 16, v25
	v_fmac_f32_e32 v21, v33, v25
	v_fmac_f32_e32 v24, v41, v25
	v_fma_f32 v25, v50, v25, v23
	s_waitcnt lgkmcnt(1)
	v_lshlrev_b32_e32 v27, 16, v27
	v_fmac_f32_e32 v21, v31, v27
	v_fmac_f32_e32 v24, v33, v27
	v_fmac_f32_e32 v25, v41, v27
	v_fma_f32 v27, v50, v27, v23
	s_waitcnt lgkmcnt(0)
	v_lshlrev_b32_e32 v30, 16, v30
	v_fmac_f32_e32 v21, v38, v30
	v_fmac_f32_e32 v24, v31, v30
	v_fmac_f32_e32 v25, v33, v30
	v_fmac_f32_e32 v27, v41, v30
	ds_read_u16 v30, v29 offset:5120
	v_ashrrev_i32_e32 v19, 5, v22
	v_and_b32_e32 v20, -2, v19
	v_add_u32_e32 v18, s4, v18
	v_lshl_add_u32 v22, v22, 2, s4
	s_waitcnt lgkmcnt(0)
	v_lshlrev_b32_e32 v30, 16, v30
	v_fmac_f32_e32 v21, v36, v30
	v_fmac_f32_e32 v24, v38, v30
	v_fmac_f32_e32 v25, v31, v30
	v_fmac_f32_e32 v27, v33, v30
	ds_read_u16 v30, v29 offset:6144
	v_cmp_gt_i32_e32 vcc, 4, v20
	s_waitcnt lgkmcnt(0)
	v_lshlrev_b32_e32 v30, 16, v30
	v_fmac_f32_e32 v21, v34, v30
	v_fmac_f32_e32 v24, v36, v30
	v_fmac_f32_e32 v25, v38, v30
	v_fmac_f32_e32 v27, v31, v30
	ds_read_u16 v100, v29 offset:7168
	ds_read_u16 v101, v29 offset:8192
	ds_read_u16 v102, v29 offset:9216
	ds_read_u16 v103, v29 offset:10240
	ds_read_u16 v104, v29 offset:11264
	ds_read_u16 v105, v29 offset:12288
	ds_read_u16 v106, v29 offset:13312
	ds_read_u16 v107, v29 offset:14336
	s_waitcnt lgkmcnt(7)
	v_lshlrev_b32_e32 v30, 16, v100
	ds_read_u16 v100, v29 offset:15360
	v_fmac_f32_e32 v21, v32, v30
	v_fmac_f32_e32 v24, v34, v30
	v_fmac_f32_e32 v25, v36, v30
	v_fmac_f32_e32 v27, v38, v30
	s_waitcnt lgkmcnt(7)
	v_lshlrev_b32_e32 v30, 16, v101
	ds_read_u16 v101, v29 offset:16384
	v_fmac_f32_e32 v21, v40, v30
	v_fmac_f32_e32 v24, v32, v30
	v_fmac_f32_e32 v25, v34, v30
	v_fmac_f32_e32 v27, v36, v30
	s_waitcnt lgkmcnt(7)
	v_lshlrev_b32_e32 v30, 16, v102
	ds_read_u16 v102, v29 offset:17408
	v_fmac_f32_e32 v21, v39, v30
	v_fmac_f32_e32 v24, v40, v30
	v_fmac_f32_e32 v25, v32, v30
	v_fmac_f32_e32 v27, v34, v30
	s_waitcnt lgkmcnt(7)
	v_lshlrev_b32_e32 v30, 16, v103
	ds_read_u16 v103, v29 offset:18432
	v_fmac_f32_e32 v21, v37, v30
	v_fmac_f32_e32 v24, v39, v30
	v_fmac_f32_e32 v25, v40, v30
	v_fmac_f32_e32 v27, v32, v30
	s_waitcnt lgkmcnt(7)
	v_lshlrev_b32_e32 v30, 16, v104
	ds_read_u16 v104, v29 offset:19456
	v_fmac_f32_e32 v21, v35, v30
	v_fmac_f32_e32 v24, v37, v30
	v_fmac_f32_e32 v25, v39, v30
	v_fmac_f32_e32 v27, v40, v30
	s_waitcnt lgkmcnt(7)
	v_lshlrev_b32_e32 v30, 16, v105
	ds_read_u16 v105, v29 offset:20480
	v_fmac_f32_e32 v21, v47, v30
	v_fmac_f32_e32 v24, v35, v30
	v_fmac_f32_e32 v25, v37, v30
	v_fmac_f32_e32 v27, v39, v30
	s_waitcnt lgkmcnt(7)
	v_lshlrev_b32_e32 v30, 16, v106
	ds_read_u16 v106, v29 offset:21504
	v_fmac_f32_e32 v21, v45, v30
	v_fmac_f32_e32 v24, v47, v30
	v_fmac_f32_e32 v25, v35, v30
	v_fmac_f32_e32 v27, v37, v30
	s_waitcnt lgkmcnt(7)
	v_lshlrev_b32_e32 v30, 16, v107
	ds_read_u16 v107, v29 offset:22528
	v_fmac_f32_e32 v21, v44, v30
	v_fmac_f32_e32 v24, v45, v30
	v_fmac_f32_e32 v25, v47, v30
	v_fmac_f32_e32 v27, v35, v30
	s_waitcnt lgkmcnt(7)
	v_lshlrev_b32_e32 v30, 16, v100
	ds_read_u16 v100, v29 offset:23552
	v_fmac_f32_e32 v21, v43, v30
	v_fmac_f32_e32 v24, v44, v30
	v_fmac_f32_e32 v25, v45, v30
	v_fmac_f32_e32 v27, v47, v30
	s_waitcnt lgkmcnt(7)
	v_lshlrev_b32_e32 v30, 16, v101
	ds_read_u16 v101, v29 offset:24576
	v_fmac_f32_e32 v21, v46, v30
	v_fmac_f32_e32 v24, v43, v30
	v_fmac_f32_e32 v25, v44, v30
	v_fmac_f32_e32 v27, v45, v30
	s_waitcnt lgkmcnt(7)
	v_lshlrev_b32_e32 v30, 16, v102
	ds_read_u16 v102, v29 offset:25600
	v_fmac_f32_e32 v21, v56, v30
	v_fmac_f32_e32 v24, v46, v30
	v_fmac_f32_e32 v25, v43, v30
	v_fmac_f32_e32 v27, v44, v30
	s_waitcnt lgkmcnt(7)
	v_lshlrev_b32_e32 v30, 16, v103
	ds_read_u16 v103, v29 offset:26624
	v_fmac_f32_e32 v21, v57, v30
	v_fmac_f32_e32 v24, v56, v30
	v_fmac_f32_e32 v25, v46, v30
	v_fmac_f32_e32 v27, v43, v30
	s_waitcnt lgkmcnt(7)
	v_lshlrev_b32_e32 v30, 16, v104
	ds_read_u16 v104, v29 offset:27648
	v_fmac_f32_e32 v21, v52, v30
	v_fmac_f32_e32 v24, v57, v30
	v_fmac_f32_e32 v25, v56, v30
	v_fmac_f32_e32 v27, v46, v30
	s_waitcnt lgkmcnt(7)
	v_lshlrev_b32_e32 v30, 16, v105
	ds_read_u16 v105, v29 offset:28672
	v_fmac_f32_e32 v21, v53, v30
	v_fmac_f32_e32 v24, v52, v30
	v_fmac_f32_e32 v25, v57, v30
	v_fmac_f32_e32 v27, v56, v30
	s_waitcnt lgkmcnt(7)
	v_lshlrev_b32_e32 v30, 16, v106
	ds_read_u16 v106, v29 offset:29696
	v_fmac_f32_e32 v21, v49, v30
	v_fmac_f32_e32 v24, v53, v30
	v_fmac_f32_e32 v25, v52, v30
	v_fmac_f32_e32 v27, v57, v30
	s_waitcnt lgkmcnt(7)
	v_lshlrev_b32_e32 v30, 16, v107
	ds_read_u16 v107, v29 offset:30720
	v_fmac_f32_e32 v21, v55, v30
	v_fmac_f32_e32 v24, v49, v30
	v_fmac_f32_e32 v25, v53, v30
	v_fmac_f32_e32 v27, v52, v30
	s_waitcnt lgkmcnt(7)
	v_lshlrev_b32_e32 v30, 16, v100
	ds_read_u16 v100, v29 offset:31744
	v_fmac_f32_e32 v21, v51, v30
	v_fmac_f32_e32 v24, v55, v30
	v_fmac_f32_e32 v25, v49, v30
	v_fmac_f32_e32 v27, v53, v30
	s_waitcnt lgkmcnt(7)
	v_lshlrev_b32_e32 v30, 16, v101
	ds_read_u16 v101, v29 offset:32768
	v_fmac_f32_e32 v21, v58, v30
	v_fmac_f32_e32 v24, v51, v30
	v_fmac_f32_e32 v25, v55, v30
	v_fmac_f32_e32 v27, v49, v30
	s_waitcnt lgkmcnt(7)
	v_lshlrev_b32_e32 v30, 16, v102
	v_fmac_f32_e32 v21, v54, v30
	v_fmac_f32_e32 v24, v58, v30
	v_fmac_f32_e32 v25, v51, v30
	v_fmac_f32_e32 v27, v55, v30
	s_waitcnt lgkmcnt(6)
	v_lshlrev_b32_e32 v30, 16, v103
	v_fmac_f32_e32 v21, v62, v30
	v_fmac_f32_e32 v24, v54, v30
	v_fmac_f32_e32 v25, v58, v30
	v_fmac_f32_e32 v27, v51, v30
	s_waitcnt lgkmcnt(5)
	v_lshlrev_b32_e32 v30, 16, v104
	v_fmac_f32_e32 v21, v60, v30
	v_fmac_f32_e32 v24, v62, v30
	v_fmac_f32_e32 v25, v54, v30
	v_fmac_f32_e32 v27, v58, v30
	s_waitcnt lgkmcnt(4)
	v_lshlrev_b32_e32 v30, 16, v105
	v_fmac_f32_e32 v21, v61, v30
	v_fmac_f32_e32 v24, v60, v30
	v_fmac_f32_e32 v25, v62, v30
	v_fmac_f32_e32 v27, v54, v30
	s_waitcnt lgkmcnt(3)
	v_lshlrev_b32_e32 v30, 16, v106
	v_fmac_f32_e32 v21, v28, v30
	v_fmac_f32_e32 v24, v61, v30
	v_fmac_f32_e32 v25, v60, v30
	v_fmac_f32_e32 v27, v62, v30
	s_waitcnt lgkmcnt(2)
	v_lshlrev_b32_e32 v30, 16, v107
	v_fmac_f32_e32 v21, v26, v30
	v_fmac_f32_e32 v24, v28, v30
	v_fmac_f32_e32 v25, v61, v30
	v_fmac_f32_e32 v27, v60, v30
	s_waitcnt lgkmcnt(1)
	v_lshlrev_b32_e32 v30, 16, v100
	v_fmac_f32_e32 v24, v26, v30
	v_fmac_f32_e32 v25, v28, v30
	v_fmac_f32_e32 v27, v61, v30
	s_waitcnt lgkmcnt(0)
	v_lshlrev_b32_e32 v30, 16, v101
	v_fmac_f32_e32 v27, v28, v30
	ds_read_u16 v28, v29 offset:33792
	v_fmac_f32_e32 v25, v26, v30
	s_waitcnt lgkmcnt(0)
	v_lshlrev_b32_e32 v28, 16, v28
	v_fmac_f32_e32 v27, v26, v28
	ds_write2st64_b32 v22, v21, v24 offset1:8
	ds_write2st64_b32 v22, v25, v27 offset0:16 offset1:24
	ds_write2st64_b32 v22, v23, v23 offset0:32 offset1:40
	ds_write2st64_b32 v22, v23, v23 offset0:48 offset1:56
	ds_write2st64_b32 v22, v23, v23 offset0:64 offset1:72
	ds_write2st64_b32 v22, v23, v23 offset0:80 offset1:88
	ds_write2st64_b32 v22, v23, v23 offset0:96 offset1:104
	ds_write2st64_b32 v22, v23, v23 offset0:112 offset1:120
	s_waitcnt lgkmcnt(0)
	s_barrier
	s_and_saveexec_b64 s[10:11], vcc
	s_cbranch_execz .LBB0_2188
	v_lshl_add_u32 v21, v20, 11, v18
	ds_read_b128 v[22:25], v21
	ds_read_b128 v[26:29], v21 offset:16
	v_readlane_b32 s2, v253, 21
	s_waitcnt lgkmcnt(1)
	v_mov_b32_e32 v30, v23
	v_mov_b32_e32 v31, v24
	v_mov_b32_e32 v32, v22
	v_mov_b32_e32 v33, v25
	v_pk_add_f32 v[30:31], v[30:31], v[32:33]
	s_waitcnt lgkmcnt(0)
	v_mov_b32_e32 v32, v28
	v_mov_b32_e32 v33, v26
	v_mov_b32_e32 v34, v29
	v_mov_b32_e32 v35, v27
	v_pk_add_f32 v[32:33], v[32:33], v[34:35]
	v_add_f32_e32 v21, v30, v31
	v_add_f32_e32 v21, v21, v33
	v_add_f32_e32 v21, v32, v21
	v_and_b32_e32 v31, 64, v214
	v_xor_b32_e32 v30, 16, v214
	v_add_f32_dpp v21, v21, v21 quad_perm:[1,0,3,2] row_mask:0xf bank_mask:0xf bound_ctrl:1
	v_add_u32_e32 v31, 64, v31
	v_cmp_lt_i32_e32 vcc, v30, v31
	v_add_f32_dpp v21, v21, v21 quad_perm:[2,3,0,1] row_mask:0xf bank_mask:0xf bound_ctrl:1
	v_add_u32_e32 v20, s2, v20
	v_cndmask_b32_e32 v30, v214, v30, vcc
	v_add_f32_dpp v21, v21, v21 row_half_mirror row_mask:0xf bank_mask:0xf bound_ctrl:1
	v_lshlrev_b32_e32 v38, 2, v30
	v_readlane_b32 s2, v255, 30
	v_add_f32_dpp v21, v21, v21 row_mirror row_mask:0xf bank_mask:0xf bound_ctrl:1
	ds_bpermute_b32 v30, v38, v21
	v_readlane_b32 s3, v255, 31
	s_waitcnt lgkmcnt(0)
	v_add_f32_e32 v21, v21, v30
	v_xor_b32_e32 v30, 32, v214
	v_cmp_lt_i32_e32 vcc, v30, v31
	s_nop 1
	v_cndmask_b32_e32 v30, v214, v30, vcc
	v_lshlrev_b32_e32 v39, 2, v30
	ds_bpermute_b32 v30, v39, v21
	s_waitcnt lgkmcnt(0)
	v_add_f32_e32 v21, v21, v30
	v_fmamk_f32 v23, v21, 0xbb000000, v23
	v_fmamk_f32 v22, v21, 0xbb000000, v22
	v_fmamk_f32 v25, v21, 0xbb000000, v25
	v_fmac_f32_e32 v24, 0xbb000000, v21
	v_pk_mul_f32 v[30:31], v[24:25], v[24:25]
	v_pk_mul_f32 v[32:33], v[22:23], v[22:23]
	v_fmamk_f32 v27, v21, 0xbb000000, v27
	v_fmamk_f32 v26, v21, 0xbb000000, v26
	v_fmamk_f32 v29, v21, 0xbb000000, v29
	v_fmac_f32_e32 v28, 0xbb000000, v21
	v_pk_mov_b32 v[34:35], v[32:33], v[30:31] op_sel:[1,0]
	v_mov_b32_e32 v33, v31
	v_pk_add_f32 v[30:31], v[34:35], v[32:33]
	v_pk_mul_f32 v[32:33], v[28:29], v[28:29]
	v_pk_mul_f32 v[34:35], v[26:27], v[26:27]
	v_mov_b32_e32 v36, v32
	v_mov_b32_e32 v37, v34
	v_mov_b32_e32 v34, v33
	v_pk_add_f32 v[32:33], v[36:37], v[34:35]
	v_add_f32_e32 v21, v30, v31
	v_add_f32_e32 v21, v33, v21
	v_add_f32_e32 v21, v32, v21
	s_nop 1
	v_add_f32_dpp v21, v21, v21 quad_perm:[1,0,3,2] row_mask:0xf bank_mask:0xf bound_ctrl:1
	s_nop 1
	v_add_f32_dpp v21, v21, v21 quad_perm:[2,3,0,1] row_mask:0xf bank_mask:0xf bound_ctrl:1
	s_nop 1
	v_add_f32_dpp v21, v21, v21 row_half_mirror row_mask:0xf bank_mask:0xf bound_ctrl:1
	s_nop 1
	v_add_f32_dpp v21, v21, v21 row_mirror row_mask:0xf bank_mask:0xf bound_ctrl:1
	ds_bpermute_b32 v30, v38, v21
	s_waitcnt lgkmcnt(0)
	v_add_f32_e32 v21, v21, v30
	ds_bpermute_b32 v30, v39, v21
	s_waitcnt lgkmcnt(0)
	v_add_f32_e32 v21, v21, v30
	v_fmamk_f32 v21, v21, 0x3b000000, v1
	v_mul_f32_e32 v30, 0x4b800000, v21
	v_cmp_gt_f32_e32 vcc, s77, v21
	s_nop 1
	v_cndmask_b32_e32 v21, v21, v30, vcc
	v_rsq_f32_e32 v21, v21
	s_nop 0
	v_mul_f32_e32 v30, 0x45800000, v21
	v_cndmask_b32_e32 v30, v21, v30, vcc
	v_pk_mul_f32 v[22:23], v[22:23], v[30:31] op_sel_hi:[1,0]
	v_pk_mul_f32 v[26:27], v[26:27], v[30:31] op_sel_hi:[1,0]
	s_waitcnt vmcnt(0)
	v_pk_fma_f32 v[22:23], v[10:11], v[22:23], v[14:15]
	v_pk_fma_f32 v[26:27], v[2:3], v[26:27], v[6:7]
	v_mul_f32_e32 v21, 0xbfb8aa3b, v22
	v_pk_mul_f32 v[24:25], v[24:25], v[30:31] op_sel_hi:[1,0]
	v_pk_mul_f32 v[28:29], v[28:29], v[30:31] op_sel_hi:[1,0]
	v_exp_f32_e32 v21, v21
	v_mul_f32_e32 v30, 0xbfb8aa3b, v26
	v_exp_f32_e32 v31, v30
	v_mul_f32_e32 v32, 0xbfb8aa3b, v27
	v_add_f32_e32 v21, 1.0, v21
	v_rcp_f32_e32 v30, v21
	v_add_f32_e32 v21, 1.0, v31
	v_mul_f32_e32 v31, 0xbfb8aa3b, v23
	v_exp_f32_e32 v31, v31
	v_exp_f32_e32 v33, v32
	v_pk_fma_f32 v[24:25], v[12:13], v[24:25], v[16:17]
	v_rcp_f32_e32 v32, v21
	v_add_f32_e32 v21, 1.0, v31
	v_pk_fma_f32 v[28:29], v[4:5], v[28:29], v[8:9]
	v_rcp_f32_e32 v31, v21
	v_add_f32_e32 v21, 1.0, v33
	v_mul_f32_e32 v33, 0xbfb8aa3b, v24
	v_exp_f32_e32 v34, v33
	v_mul_f32_e32 v33, 0xbfb8aa3b, v28
	v_exp_f32_e32 v35, v33
	v_rcp_f32_e32 v33, v21
	v_add_f32_e32 v21, 1.0, v34
	v_rcp_f32_e32 v34, v21
	v_add_f32_e32 v21, 1.0, v35
	v_mul_f32_e32 v35, 0xbfb8aa3b, v25
	v_exp_f32_e32 v35, v35
	v_mul_f32_e32 v36, 0xbfb8aa3b, v29
	v_exp_f32_e32 v37, v36
	v_rcp_f32_e32 v36, v21
	v_add_f32_e32 v21, 1.0, v35
	v_rcp_f32_e32 v35, v21
	v_add_f32_e32 v21, 1.0, v37
	v_rcp_f32_e32 v37, v21
	v_ashrrev_i32_e32 v21, 31, v20
	v_lshlrev_b64 v[20:21], 11, v[20:21]
	v_pk_mul_f32 v[22:23], v[22:23], v[30:31]
	v_pk_mul_f32 v[26:27], v[26:27], v[32:33]
	v_pk_mul_f32 v[24:25], v[24:25], v[34:35]
	v_pk_mul_f32 v[28:29], v[28:29], v[36:37]
	v_lshl_add_u64 v[20:21], s[2:3], 0, v[20:21]
	v_cvt_pk_bf16_f32 v22, v22, v23
	v_cvt_pk_bf16_f32 v23, v24, v25
	v_cvt_pk_bf16_f32 v24, v26, v27
	v_cvt_pk_bf16_f32 v25, v28, v29
	v_lshl_add_u64 v[20:21], v[20:21], 0, v[98:99]
	global_store_dwordx4 v[20:21], v[22:25], off offset:1024
